# combo10 + in-proj epilogue: each 1 KiB store transposed through a private LDS slot so a lane quad writes 64 contiguous bytes; stores deferred one pair
# speedup vs baseline: 1.0120x; 1.0070x over previous
.LBB0_247:
	s_mov_b32 s17, s61
	v_mbcnt_lo_u32_b32 v128, -1, 0
	v_mbcnt_hi_u32_b32 v128, -1, v128
	v_and_b32_e32 v188, 15, v128
	v_lshrrev_b32_e32 v189, 4, v128
	v_bfe_u32 v186, v128, 1, 2
	v_xor_b32_e32 v186, v189, v186
	v_lshlrev_b32_e32 v186, 4, v186
	v_lshl_or_b32 v186, v188, 6, v186
	s_lshl_b32 s74, s17, 10
	s_add_i32 s74, s74, 0x21000
	v_add_u32_e32 v186, s74, v186
	v_lshrrev_b32_e32 v188, 2, v128
	v_and_b32_e32 v189, 3, v128
	v_bfe_u32 v187, v128, 3, 2
	v_xor_b32_e32 v187, v189, v187
	v_lshlrev_b32_e32 v187, 4, v187
	v_lshl_or_b32 v187, v188, 6, v187
	v_add_u32_e32 v187, s74, v187
	v_lshl_or_b32 v128, v189, 4, v188
	s_cmp_lt_i32 s59, 5
	v_lshl_or_b32 v129, s17, 6, v128
	s_mov_b32 s64, 0x3fb8aa3b
	v_readfirstlane_b32 s19, v129
	v_mov_b32_e32 v218, v183
	s_cbranch_scc1 .LBB0_250
	s_cmp_gt_i32 s59, 7
	s_cbranch_scc0 .LBB0_251
	s_cmp_lg_u32 s59, 8
	s_mov_b64 s[22:23], -1
	s_cselect_b64 s[24:25], -1, 0
	s_cbranch_execz .LBB0_252
	s_branch .LBB0_253

.LBB0_255:
	v_and_b32_e32 v129, 15, v128
	s_ashr_i32 s17, s19, 8
	s_bfe_u32 s19, s19, 0x20006
	v_bfe_u32 v140, v128, 4, 2
	s_andn2_b64 vcc, exec, s[24:25]
	v_lshlrev_b32_e32 v138, 1, v129
	v_and_b32_e32 v139, 3, v128
	s_cbranch_vccnz .LBB0_258
	s_lshl_b32 s24, s59, 8
	s_lshl_b32 s25, s19, 5
	s_lshl_b32 s22, s57, 8
	s_lshl_b32 s23, s17, 6
	s_or_b32 s24, s25, s24
	v_lshl_or_b32 v130, v140, 3, s24
	v_and_b32_e32 v128, 24, v138
	s_add_i32 s23, s23, s22
	v_or3_b32 v141, s23, v139, v128
	v_ashrrev_i32_e32 v131, 31, v130
	v_mov_b64_e32 v[128:129], s[12:13]
	v_mad_i64_i32 v[142:143], s[22:23], v141, s71, v[128:129]
	v_lshlrev_b64 v[130:131], 1, v[130:131]
	v_lshl_add_u64 v[146:147], v[142:143], 0, v[130:131]
	v_pk_mul_f32 v[142:143], v[124:125], s[48:49] op_sel_hi:[1,0]
	v_pk_mul_f32 v[144:145], v[126:127], s[48:49] op_sel_hi:[1,0]
	v_cvt_pk_bf16_f32 v142, v142, v143
	v_pk_mul_f32 v[148:149], v[122:123], s[48:49] op_sel_hi:[1,0]
	v_cvt_pk_bf16_f32 v143, v144, v145
	v_pk_mul_f32 v[150:151], v[120:121], s[48:49] op_sel_hi:[1,0]
	s_nop 0
	v_cvt_pk_bf16_f32 v144, v150, v151
	v_cvt_pk_bf16_f32 v145, v148, v149
	ds_write_b128 v186, v[142:145]
	ds_read_b128 v[190:193], v187
	v_pk_mul_f32 v[148:149], v[114:115], s[48:49] op_sel_hi:[1,0]
	v_pk_mul_f32 v[150:151], v[112:113], s[48:49] op_sel_hi:[1,0]
	v_pk_mul_f32 v[142:143], v[116:117], s[48:49] op_sel_hi:[1,0]
	v_pk_mul_f32 v[144:145], v[118:119], s[48:49] op_sel_hi:[1,0]
	v_cvt_pk_bf16_f32 v142, v142, v143
	s_nop 0
	v_cvt_pk_bf16_f32 v143, v144, v145
	v_cvt_pk_bf16_f32 v144, v150, v151
	v_cvt_pk_bf16_f32 v145, v148, v149
	ds_write_b128 v186, v[142:145]
	ds_read_b128 v[194:197], v187
	v_mov_b64_e32 v[214:215], v[146:147]
	v_pk_mul_f32 v[148:149], v[106:107], s[48:49] op_sel_hi:[1,0]
	v_pk_mul_f32 v[150:151], v[104:105], s[48:49] op_sel_hi:[1,0]
	v_or_b32_e32 v142, 4, v141
	v_mad_i64_i32 v[142:143], s[22:23], v142, s71, v[128:129]
	v_lshl_add_u64 v[146:147], v[142:143], 0, v[130:131]
	v_pk_mul_f32 v[142:143], v[108:109], s[48:49] op_sel_hi:[1,0]
	v_pk_mul_f32 v[144:145], v[110:111], s[48:49] op_sel_hi:[1,0]
	v_cvt_pk_bf16_f32 v142, v142, v143
	s_nop 0
	v_cvt_pk_bf16_f32 v143, v144, v145
	v_cvt_pk_bf16_f32 v144, v150, v151
	v_cvt_pk_bf16_f32 v145, v148, v149
	ds_write_b128 v186, v[142:145]
	ds_read_b128 v[198:201], v187
	v_pk_mul_f32 v[148:149], v[98:99], s[48:49] op_sel_hi:[1,0]
	v_pk_mul_f32 v[150:151], v[96:97], s[48:49] op_sel_hi:[1,0]
	v_pk_mul_f32 v[142:143], v[100:101], s[48:49] op_sel_hi:[1,0]
	v_pk_mul_f32 v[144:145], v[102:103], s[48:49] op_sel_hi:[1,0]
	v_cvt_pk_bf16_f32 v142, v142, v143
	s_nop 0
	v_cvt_pk_bf16_f32 v143, v144, v145
	v_cvt_pk_bf16_f32 v144, v150, v151
	v_cvt_pk_bf16_f32 v145, v148, v149
	ds_write_b128 v186, v[142:145]
	ds_read_b128 v[202:205], v187
	v_mov_b64_e32 v[216:217], v[146:147]
	s_waitcnt lgkmcnt(4)
	global_store_dwordx4 v[214:215], v[190:193], off
	global_store_dwordx4 v[214:215], v[194:197], off offset:256
	v_pk_mul_f32 v[148:149], v[90:91], s[48:49] op_sel_hi:[1,0]
	v_pk_mul_f32 v[150:151], v[88:89], s[48:49] op_sel_hi:[1,0]
	v_or_b32_e32 v142, 32, v141
	v_mad_i64_i32 v[142:143], s[22:23], v142, s71, v[128:129]
	v_lshl_add_u64 v[146:147], v[142:143], 0, v[130:131]
	v_pk_mul_f32 v[142:143], v[92:93], s[48:49] op_sel_hi:[1,0]
	v_pk_mul_f32 v[144:145], v[94:95], s[48:49] op_sel_hi:[1,0]
	v_cvt_pk_bf16_f32 v142, v142, v143
	s_nop 0
	v_cvt_pk_bf16_f32 v143, v144, v145
	v_cvt_pk_bf16_f32 v144, v150, v151
	v_cvt_pk_bf16_f32 v145, v148, v149
	ds_write_b128 v186, v[142:145]
	ds_read_b128 v[190:193], v187
	v_pk_mul_f32 v[148:149], v[82:83], s[48:49] op_sel_hi:[1,0]
	v_pk_mul_f32 v[150:151], v[80:81], s[48:49] op_sel_hi:[1,0]
	v_pk_mul_f32 v[142:143], v[84:85], s[48:49] op_sel_hi:[1,0]
	v_pk_mul_f32 v[144:145], v[86:87], s[48:49] op_sel_hi:[1,0]
	v_cvt_pk_bf16_f32 v142, v142, v143
	s_nop 0
	v_cvt_pk_bf16_f32 v143, v144, v145
	v_cvt_pk_bf16_f32 v144, v150, v151
	v_cvt_pk_bf16_f32 v145, v148, v149
	ds_write_b128 v186, v[142:145]
	ds_read_b128 v[194:197], v187
	v_mov_b64_e32 v[214:215], v[146:147]
	s_waitcnt lgkmcnt(4)
	global_store_dwordx4 v[216:217], v[198:201], off
	global_store_dwordx4 v[216:217], v[202:205], off offset:256
	v_pk_mul_f32 v[148:149], v[74:75], s[48:49] op_sel_hi:[1,0]
	v_pk_mul_f32 v[150:151], v[72:73], s[48:49] op_sel_hi:[1,0]
	v_or_b32_e32 v142, 36, v141
	v_mad_i64_i32 v[142:143], s[22:23], v142, s71, v[128:129]
	v_lshl_add_u64 v[146:147], v[142:143], 0, v[130:131]
	v_pk_mul_f32 v[142:143], v[76:77], s[48:49] op_sel_hi:[1,0]
	v_pk_mul_f32 v[144:145], v[78:79], s[48:49] op_sel_hi:[1,0]
	v_cvt_pk_bf16_f32 v142, v142, v143
	s_nop 0
	v_cvt_pk_bf16_f32 v143, v144, v145
	v_cvt_pk_bf16_f32 v144, v150, v151
	v_cvt_pk_bf16_f32 v145, v148, v149
	ds_write_b128 v186, v[142:145]
	ds_read_b128 v[198:201], v187
	v_pk_mul_f32 v[148:149], v[66:67], s[48:49] op_sel_hi:[1,0]
	v_pk_mul_f32 v[150:151], v[64:65], s[48:49] op_sel_hi:[1,0]
	v_pk_mul_f32 v[142:143], v[68:69], s[48:49] op_sel_hi:[1,0]
	v_pk_mul_f32 v[144:145], v[70:71], s[48:49] op_sel_hi:[1,0]
	v_cvt_pk_bf16_f32 v142, v142, v143
	s_nop 0
	v_cvt_pk_bf16_f32 v143, v144, v145
	v_cvt_pk_bf16_f32 v144, v150, v151
	v_cvt_pk_bf16_f32 v145, v148, v149
	ds_write_b128 v186, v[142:145]
	ds_read_b128 v[202:205], v187
	v_mov_b64_e32 v[216:217], v[146:147]
	s_waitcnt lgkmcnt(4)
	global_store_dwordx4 v[214:215], v[190:193], off
	global_store_dwordx4 v[214:215], v[194:197], off offset:256
	v_pk_mul_f32 v[148:149], v[58:59], s[48:49] op_sel_hi:[1,0]
	v_pk_mul_f32 v[150:151], v[56:57], s[48:49] op_sel_hi:[1,0]
	v_add_u32_e32 v142, 0x80, v141
	v_mad_i64_i32 v[142:143], s[22:23], v142, s71, v[128:129]
	v_lshl_add_u64 v[146:147], v[142:143], 0, v[130:131]
	v_pk_mul_f32 v[142:143], v[60:61], s[48:49] op_sel_hi:[1,0]
	v_pk_mul_f32 v[144:145], v[62:63], s[48:49] op_sel_hi:[1,0]
	v_cvt_pk_bf16_f32 v142, v142, v143
	s_nop 0
	v_cvt_pk_bf16_f32 v143, v144, v145
	v_cvt_pk_bf16_f32 v144, v150, v151
	v_cvt_pk_bf16_f32 v145, v148, v149
	ds_write_b128 v186, v[142:145]
	ds_read_b128 v[190:193], v187
	v_pk_mul_f32 v[148:149], v[50:51], s[48:49] op_sel_hi:[1,0]
	v_pk_mul_f32 v[150:151], v[48:49], s[48:49] op_sel_hi:[1,0]
	v_pk_mul_f32 v[142:143], v[52:53], s[48:49] op_sel_hi:[1,0]
	v_pk_mul_f32 v[144:145], v[54:55], s[48:49] op_sel_hi:[1,0]
	v_cvt_pk_bf16_f32 v142, v142, v143
	s_nop 0
	v_cvt_pk_bf16_f32 v143, v144, v145
	v_cvt_pk_bf16_f32 v144, v150, v151
	v_cvt_pk_bf16_f32 v145, v148, v149
	ds_write_b128 v186, v[142:145]
	ds_read_b128 v[194:197], v187
	v_mov_b64_e32 v[214:215], v[146:147]
	s_waitcnt lgkmcnt(4)
	global_store_dwordx4 v[216:217], v[198:201], off
	global_store_dwordx4 v[216:217], v[202:205], off offset:256
	v_pk_mul_f32 v[148:149], v[42:43], s[48:49] op_sel_hi:[1,0]
	v_pk_mul_f32 v[150:151], v[40:41], s[48:49] op_sel_hi:[1,0]
	v_add_u32_e32 v142, 0x84, v141
	v_mad_i64_i32 v[142:143], s[22:23], v142, s71, v[128:129]
	v_lshl_add_u64 v[146:147], v[142:143], 0, v[130:131]
	v_pk_mul_f32 v[142:143], v[44:45], s[48:49] op_sel_hi:[1,0]
	v_pk_mul_f32 v[144:145], v[46:47], s[48:49] op_sel_hi:[1,0]
	v_cvt_pk_bf16_f32 v142, v142, v143
	s_nop 0
	v_cvt_pk_bf16_f32 v143, v144, v145
	v_cvt_pk_bf16_f32 v144, v150, v151
	v_cvt_pk_bf16_f32 v145, v148, v149
	ds_write_b128 v186, v[142:145]
	ds_read_b128 v[198:201], v187
	v_pk_mul_f32 v[148:149], v[34:35], s[48:49] op_sel_hi:[1,0]
	v_pk_mul_f32 v[150:151], v[32:33], s[48:49] op_sel_hi:[1,0]
	v_pk_mul_f32 v[142:143], v[36:37], s[48:49] op_sel_hi:[1,0]
	v_pk_mul_f32 v[144:145], v[38:39], s[48:49] op_sel_hi:[1,0]
	v_cvt_pk_bf16_f32 v142, v142, v143
	s_nop 0
	v_cvt_pk_bf16_f32 v143, v144, v145
	v_cvt_pk_bf16_f32 v144, v150, v151
	v_cvt_pk_bf16_f32 v145, v148, v149
	ds_write_b128 v186, v[142:145]
	ds_read_b128 v[202:205], v187
	v_mov_b64_e32 v[216:217], v[146:147]
	s_waitcnt lgkmcnt(4)
	global_store_dwordx4 v[214:215], v[190:193], off
	global_store_dwordx4 v[214:215], v[194:197], off offset:256
	v_pk_mul_f32 v[148:149], v[26:27], s[48:49] op_sel_hi:[1,0]
	v_pk_mul_f32 v[150:151], v[24:25], s[48:49] op_sel_hi:[1,0]
	v_add_u32_e32 v142, 0xa0, v141
	v_mad_i64_i32 v[142:143], s[22:23], v142, s71, v[128:129]
	v_lshl_add_u64 v[146:147], v[142:143], 0, v[130:131]
	v_pk_mul_f32 v[142:143], v[28:29], s[48:49] op_sel_hi:[1,0]
	v_pk_mul_f32 v[144:145], v[30:31], s[48:49] op_sel_hi:[1,0]
	v_cvt_pk_bf16_f32 v142, v142, v143
	v_add_u32_e32 v141, 0xa4, v141
	v_cvt_pk_bf16_f32 v143, v144, v145
	v_cvt_pk_bf16_f32 v144, v150, v151
	v_cvt_pk_bf16_f32 v145, v148, v149
	ds_write_b128 v186, v[142:145]
	ds_read_b128 v[190:193], v187
	v_mad_i64_i32 v[128:129], s[22:23], v141, s71, v[128:129]
	s_nop 0
	v_pk_mul_f32 v[142:143], v[20:21], s[48:49] op_sel_hi:[1,0]
	v_pk_mul_f32 v[144:145], v[22:23], s[48:49] op_sel_hi:[1,0]
	v_cvt_pk_bf16_f32 v142, v142, v143
	v_pk_mul_f32 v[148:149], v[18:19], s[48:49] op_sel_hi:[1,0]
	v_cvt_pk_bf16_f32 v143, v144, v145
	v_pk_mul_f32 v[150:151], v[16:17], s[48:49] op_sel_hi:[1,0]
	s_nop 0
	v_cvt_pk_bf16_f32 v144, v150, v151
	v_cvt_pk_bf16_f32 v145, v148, v149
	ds_write_b128 v186, v[142:145]
	ds_read_b128 v[194:197], v187
	v_mov_b64_e32 v[214:215], v[146:147]
	s_waitcnt lgkmcnt(4)
	global_store_dwordx4 v[216:217], v[198:201], off
	global_store_dwordx4 v[216:217], v[202:205], off offset:256
	v_pk_mul_f32 v[146:147], v[8:9], s[48:49] op_sel_hi:[1,0]
	s_nop 0
	v_lshl_add_u64 v[142:143], v[128:129], 0, v[130:131]
	v_pk_mul_f32 v[130:131], v[14:15], s[48:49] op_sel_hi:[1,0]
	v_pk_mul_f32 v[128:129], v[12:13], s[48:49] op_sel_hi:[1,0]
	v_pk_mul_f32 v[144:145], v[10:11], s[48:49] op_sel_hi:[1,0]
	v_cvt_pk_bf16_f32 v128, v128, v129
	v_cvt_pk_bf16_f32 v129, v130, v131
	v_cvt_pk_bf16_f32 v130, v146, v147
	v_pk_mul_f32 v[146:147], v[0:1], s[48:49] op_sel_hi:[1,0]
	v_cvt_pk_bf16_f32 v131, v144, v145
	ds_write_b128 v186, v[128:131]
	ds_read_b128 v[198:201], v187
	v_pk_mul_f32 v[144:145], v[2:3], s[48:49] op_sel_hi:[1,0]
	s_nop 0
	v_pk_mul_f32 v[130:131], v[6:7], s[48:49] op_sel_hi:[1,0]
	v_pk_mul_f32 v[128:129], v[4:5], s[48:49] op_sel_hi:[1,0]
	s_nop 0
	v_cvt_pk_bf16_f32 v128, v128, v129
	v_cvt_pk_bf16_f32 v129, v130, v131
	v_cvt_pk_bf16_f32 v130, v146, v147
	v_cvt_pk_bf16_f32 v131, v144, v145
	ds_write_b128 v186, v[128:131]
	ds_read_b128 v[202:205], v187
	v_mov_b64_e32 v[216:217], v[142:143]
	s_waitcnt lgkmcnt(4)
	global_store_dwordx4 v[214:215], v[190:193], off
	global_store_dwordx4 v[214:215], v[194:197], off offset:256
	s_waitcnt lgkmcnt(0)
	global_store_dwordx4 v[216:217], v[198:201], off
	global_store_dwordx4 v[216:217], v[202:205], off offset:256
	s_cbranch_execz .LBB0_259

.LBB0_259:
	s_add_i32 s22, s59, 0xfffe
	s_and_b32 s22, s22, 0xff
	s_mulk_i32 s22, 0xab
	v_lshlrev_b32_e32 v128, 3, v140
	s_lshr_b32 s22, s22, 4
	s_lshl_b32 s23, s57, 8
	v_lshl_or_b32 v128, s19, 5, v128
	s_ashr_i32 s19, s57, 3
	s_and_b32 s22, s22, 0xfe0
	s_and_b32 s23, s23, 0x700
	s_add_i32 s22, s22, s19
	v_or_b32_e32 v128, s23, v128
	s_ashr_i32 s23, s22, 31
	s_lshl_b32 s24, s17, 6
	s_ashr_i32 s25, s24, 31
	s_lshl_b64 s[22:23], s[22:23], 20
	s_add_u32 s17, s39, s22
	s_addc_u32 s19, s40, s23
	s_lshl_b64 s[22:23], s[24:25], 12
	s_add_u32 s22, s17, s22
	s_addc_u32 s23, s19, s23
	v_lshlrev_b32_e32 v184, 1, v128
	v_and_or_b32 v130, v138, 24, v139
	v_lshl_add_u64 v[128:129], s[22:23], 0, v[184:185]
	v_lshlrev_b32_e32 v184, 12, v130
	v_lshl_add_u64 v[128:129], v[128:129], 0, v[184:185]
	v_pk_mul_f32 v[126:127], v[126:127], s[48:49] op_sel_hi:[1,0]
	v_pk_mul_f32 v[124:125], v[124:125], s[48:49] op_sel_hi:[1,0]
	v_pk_mul_f32 v[130:131], v[122:123], s[48:49] op_sel_hi:[1,0]
	v_pk_mul_f32 v[122:123], v[120:121], s[48:49] op_sel_hi:[1,0]
	v_cvt_pk_bf16_f32 v120, v124, v125
	v_cvt_pk_bf16_f32 v121, v126, v127
	v_pk_mul_f32 v[118:119], v[118:119], s[48:49] op_sel_hi:[1,0]
	v_cvt_pk_bf16_f32 v122, v122, v123
	v_cvt_pk_bf16_f32 v123, v130, v131
	ds_write_b128 v186, v[120:123]
	ds_read_b128 v[190:193], v187
	v_pk_mul_f32 v[116:117], v[116:117], s[48:49] op_sel_hi:[1,0]
	v_pk_mul_f32 v[108:109], v[108:109], s[48:49] op_sel_hi:[1,0]
	v_pk_mul_f32 v[120:121], v[114:115], s[48:49] op_sel_hi:[1,0]
	v_pk_mul_f32 v[114:115], v[112:113], s[48:49] op_sel_hi:[1,0]
	v_cvt_pk_bf16_f32 v112, v116, v117
	v_cvt_pk_bf16_f32 v113, v118, v119
	s_movk_i32 s17, 0x4000
	v_cvt_pk_bf16_f32 v114, v114, v115
	v_cvt_pk_bf16_f32 v115, v120, v121
	ds_write_b128 v186, v[112:115]
	ds_read_b128 v[194:197], v187
	v_mov_b64_e32 v[214:215], v[128:129]
	v_pk_mul_f32 v[110:111], v[110:111], s[48:49] op_sel_hi:[1,0]
	v_pk_mul_f32 v[102:103], v[102:103], s[48:49] op_sel_hi:[1,0]
	v_pk_mul_f32 v[112:113], v[106:107], s[48:49] op_sel_hi:[1,0]
	v_pk_mul_f32 v[106:107], v[104:105], s[48:49] op_sel_hi:[1,0]
	v_cvt_pk_bf16_f32 v104, v108, v109
	v_add_co_u32_e32 v108, vcc, s17, v128
	v_cvt_pk_bf16_f32 v105, v110, v111
	v_cvt_pk_bf16_f32 v106, v106, v107
	v_cvt_pk_bf16_f32 v107, v112, v113
	v_pk_mul_f32 v[100:101], v[100:101], s[48:49] op_sel_hi:[1,0]
	s_nop 0
	v_addc_co_u32_e32 v109, vcc, 0, v129, vcc
	ds_write_b128 v186, v[104:107]
	ds_read_b128 v[198:201], v187
	v_pk_mul_f32 v[92:93], v[92:93], s[48:49] op_sel_hi:[1,0]
	s_mov_b32 s17, 0x20000
	v_pk_mul_f32 v[104:105], v[98:99], s[48:49] op_sel_hi:[1,0]
	v_pk_mul_f32 v[98:99], v[96:97], s[48:49] op_sel_hi:[1,0]
	v_cvt_pk_bf16_f32 v96, v100, v101
	v_cvt_pk_bf16_f32 v97, v102, v103
	v_pk_mul_f32 v[94:95], v[94:95], s[48:49] op_sel_hi:[1,0]
	v_cvt_pk_bf16_f32 v98, v98, v99
	v_cvt_pk_bf16_f32 v99, v104, v105
	ds_write_b128 v186, v[96:99]
	ds_read_b128 v[202:205], v187
	v_mov_b64_e32 v[216:217], v[108:109]
	s_waitcnt lgkmcnt(4)
	global_store_dwordx4 v[214:215], v[190:193], off
	global_store_dwordx4 v[214:215], v[194:197], off offset:256
	v_pk_mul_f32 v[86:87], v[86:87], s[48:49] op_sel_hi:[1,0]
	v_pk_mul_f32 v[84:85], v[84:85], s[48:49] op_sel_hi:[1,0]
	v_pk_mul_f32 v[96:97], v[90:91], s[48:49] op_sel_hi:[1,0]
	v_pk_mul_f32 v[90:91], v[88:89], s[48:49] op_sel_hi:[1,0]
	v_cvt_pk_bf16_f32 v88, v92, v93
	v_add_co_u32_e32 v92, vcc, s17, v128
	v_cvt_pk_bf16_f32 v89, v94, v95
	v_cvt_pk_bf16_f32 v90, v90, v91
	v_cvt_pk_bf16_f32 v91, v96, v97
	v_pk_mul_f32 v[76:77], v[76:77], s[48:49] op_sel_hi:[1,0]
	s_nop 0
	v_addc_co_u32_e32 v93, vcc, 0, v129, vcc
	ds_write_b128 v186, v[88:91]
	ds_read_b128 v[190:193], v187
	s_mov_b32 s17, 0x24000
	v_pk_mul_f32 v[78:79], v[78:79], s[48:49] op_sel_hi:[1,0]
	v_pk_mul_f32 v[88:89], v[82:83], s[48:49] op_sel_hi:[1,0]
	v_pk_mul_f32 v[82:83], v[80:81], s[48:49] op_sel_hi:[1,0]
	v_cvt_pk_bf16_f32 v80, v84, v85
	v_cvt_pk_bf16_f32 v81, v86, v87
	v_pk_mul_f32 v[70:71], v[70:71], s[48:49] op_sel_hi:[1,0]
	v_cvt_pk_bf16_f32 v82, v82, v83
	v_cvt_pk_bf16_f32 v83, v88, v89
	ds_write_b128 v186, v[80:83]
	ds_read_b128 v[194:197], v187
	v_mov_b64_e32 v[214:215], v[92:93]
	s_waitcnt lgkmcnt(4)
	global_store_dwordx4 v[216:217], v[198:201], off
	global_store_dwordx4 v[216:217], v[202:205], off offset:256
	v_pk_mul_f32 v[68:69], v[68:69], s[48:49] op_sel_hi:[1,0]
	v_pk_mul_f32 v[60:61], v[60:61], s[48:49] op_sel_hi:[1,0]
	v_pk_mul_f32 v[80:81], v[74:75], s[48:49] op_sel_hi:[1,0]
	v_pk_mul_f32 v[74:75], v[72:73], s[48:49] op_sel_hi:[1,0]
	v_cvt_pk_bf16_f32 v72, v76, v77
	v_add_co_u32_e32 v76, vcc, s17, v128
	v_cvt_pk_bf16_f32 v73, v78, v79
	v_cvt_pk_bf16_f32 v74, v74, v75
	v_cvt_pk_bf16_f32 v75, v80, v81
	s_mov_b32 s17, 0x80000
	s_nop 0
	v_addc_co_u32_e32 v77, vcc, 0, v129, vcc
	ds_write_b128 v186, v[72:75]
	ds_read_b128 v[198:201], v187
	v_pk_mul_f32 v[62:63], v[62:63], s[48:49] op_sel_hi:[1,0]
	v_pk_mul_f32 v[54:55], v[54:55], s[48:49] op_sel_hi:[1,0]
	v_pk_mul_f32 v[72:73], v[66:67], s[48:49] op_sel_hi:[1,0]
	v_pk_mul_f32 v[66:67], v[64:65], s[48:49] op_sel_hi:[1,0]
	v_cvt_pk_bf16_f32 v64, v68, v69
	v_cvt_pk_bf16_f32 v65, v70, v71
	v_pk_mul_f32 v[52:53], v[52:53], s[48:49] op_sel_hi:[1,0]
	v_cvt_pk_bf16_f32 v66, v66, v67
	v_cvt_pk_bf16_f32 v67, v72, v73
	ds_write_b128 v186, v[64:67]
	ds_read_b128 v[202:205], v187
	v_mov_b64_e32 v[216:217], v[76:77]
	s_waitcnt lgkmcnt(4)
	global_store_dwordx4 v[214:215], v[190:193], off
	global_store_dwordx4 v[214:215], v[194:197], off offset:256
	v_pk_mul_f32 v[44:45], v[44:45], s[48:49] op_sel_hi:[1,0]
	v_pk_mul_f32 v[46:47], v[46:47], s[48:49] op_sel_hi:[1,0]
	v_pk_mul_f32 v[64:65], v[58:59], s[48:49] op_sel_hi:[1,0]
	v_pk_mul_f32 v[58:59], v[56:57], s[48:49] op_sel_hi:[1,0]
	v_cvt_pk_bf16_f32 v56, v60, v61
	v_add_co_u32_e32 v60, vcc, s17, v128
	v_cvt_pk_bf16_f32 v57, v62, v63
	v_cvt_pk_bf16_f32 v58, v58, v59
	v_cvt_pk_bf16_f32 v59, v64, v65
	s_mov_b32 s17, 0x84000
	s_nop 0
	v_addc_co_u32_e32 v61, vcc, 0, v129, vcc
	ds_write_b128 v186, v[56:59]
	ds_read_b128 v[190:193], v187
	v_pk_mul_f32 v[38:39], v[38:39], s[48:49] op_sel_hi:[1,0]
	v_pk_mul_f32 v[36:37], v[36:37], s[48:49] op_sel_hi:[1,0]
	v_pk_mul_f32 v[56:57], v[50:51], s[48:49] op_sel_hi:[1,0]
	v_pk_mul_f32 v[50:51], v[48:49], s[48:49] op_sel_hi:[1,0]
	v_cvt_pk_bf16_f32 v48, v52, v53
	v_cvt_pk_bf16_f32 v49, v54, v55
	v_pk_mul_f32 v[28:29], v[28:29], s[48:49] op_sel_hi:[1,0]
	v_cvt_pk_bf16_f32 v50, v50, v51
	v_cvt_pk_bf16_f32 v51, v56, v57
	ds_write_b128 v186, v[48:51]
	ds_read_b128 v[194:197], v187
	v_mov_b64_e32 v[214:215], v[60:61]
	s_waitcnt lgkmcnt(4)
	global_store_dwordx4 v[216:217], v[198:201], off
	global_store_dwordx4 v[216:217], v[202:205], off offset:256
	v_pk_mul_f32 v[30:31], v[30:31], s[48:49] op_sel_hi:[1,0]
	v_pk_mul_f32 v[22:23], v[22:23], s[48:49] op_sel_hi:[1,0]
	v_pk_mul_f32 v[48:49], v[42:43], s[48:49] op_sel_hi:[1,0]
	v_pk_mul_f32 v[42:43], v[40:41], s[48:49] op_sel_hi:[1,0]
	v_cvt_pk_bf16_f32 v40, v44, v45
	v_add_co_u32_e32 v44, vcc, s17, v128
	v_cvt_pk_bf16_f32 v41, v46, v47
	v_cvt_pk_bf16_f32 v42, v42, v43
	v_cvt_pk_bf16_f32 v43, v48, v49
	s_mov_b32 s17, 0xa0000
	s_nop 0
	v_addc_co_u32_e32 v45, vcc, 0, v129, vcc
	ds_write_b128 v186, v[40:43]
	ds_read_b128 v[198:201], v187
	v_pk_mul_f32 v[20:21], v[20:21], s[48:49] op_sel_hi:[1,0]
	v_pk_mul_f32 v[12:13], v[12:13], s[48:49] op_sel_hi:[1,0]
	v_pk_mul_f32 v[40:41], v[34:35], s[48:49] op_sel_hi:[1,0]
	v_pk_mul_f32 v[34:35], v[32:33], s[48:49] op_sel_hi:[1,0]
	v_cvt_pk_bf16_f32 v32, v36, v37
	v_cvt_pk_bf16_f32 v33, v38, v39
	v_pk_mul_f32 v[14:15], v[14:15], s[48:49] op_sel_hi:[1,0]
	v_cvt_pk_bf16_f32 v34, v34, v35
	v_cvt_pk_bf16_f32 v35, v40, v41
	ds_write_b128 v186, v[32:35]
	ds_read_b128 v[202:205], v187
	v_mov_b64_e32 v[216:217], v[44:45]
	s_waitcnt lgkmcnt(4)
	global_store_dwordx4 v[214:215], v[190:193], off
	global_store_dwordx4 v[214:215], v[194:197], off offset:256
	v_pk_mul_f32 v[6:7], v[6:7], s[48:49] op_sel_hi:[1,0]
	v_pk_mul_f32 v[4:5], v[4:5], s[48:49] op_sel_hi:[1,0]
	v_pk_mul_f32 v[32:33], v[26:27], s[48:49] op_sel_hi:[1,0]
	v_pk_mul_f32 v[26:27], v[24:25], s[48:49] op_sel_hi:[1,0]
	v_cvt_pk_bf16_f32 v24, v28, v29
	v_add_co_u32_e32 v28, vcc, s17, v128
	v_cvt_pk_bf16_f32 v25, v30, v31
	v_cvt_pk_bf16_f32 v26, v26, v27
	v_cvt_pk_bf16_f32 v27, v32, v33
	s_mov_b32 s17, 0xa4000
	s_nop 0
	v_addc_co_u32_e32 v29, vcc, 0, v129, vcc
	ds_write_b128 v186, v[24:27]
	ds_read_b128 v[190:193], v187
	s_nop 1
	v_pk_mul_f32 v[24:25], v[18:19], s[48:49] op_sel_hi:[1,0]
	v_pk_mul_f32 v[18:19], v[16:17], s[48:49] op_sel_hi:[1,0]
	v_cvt_pk_bf16_f32 v16, v20, v21
	v_cvt_pk_bf16_f32 v17, v22, v23
	s_nop 0
	v_cvt_pk_bf16_f32 v18, v18, v19
	v_cvt_pk_bf16_f32 v19, v24, v25
	ds_write_b128 v186, v[16:19]
	ds_read_b128 v[194:197], v187
	v_mov_b64_e32 v[214:215], v[28:29]
	s_waitcnt lgkmcnt(4)
	global_store_dwordx4 v[216:217], v[198:201], off
	global_store_dwordx4 v[216:217], v[202:205], off offset:256
	s_nop 1
	v_pk_mul_f32 v[16:17], v[10:11], s[48:49] op_sel_hi:[1,0]
	v_pk_mul_f32 v[10:11], v[8:9], s[48:49] op_sel_hi:[1,0]
	v_cvt_pk_bf16_f32 v8, v12, v13
	v_add_co_u32_e32 v12, vcc, s17, v128
	v_cvt_pk_bf16_f32 v9, v14, v15
	v_cvt_pk_bf16_f32 v10, v10, v11
	v_cvt_pk_bf16_f32 v11, v16, v17
	s_nop 1
	v_addc_co_u32_e32 v13, vcc, 0, v129, vcc
	ds_write_b128 v186, v[8:11]
	ds_read_b128 v[198:201], v187
	s_nop 1
	v_pk_mul_f32 v[8:9], v[2:3], s[48:49] op_sel_hi:[1,0]
	v_pk_mul_f32 v[2:3], v[0:1], s[48:49] op_sel_hi:[1,0]
	v_cvt_pk_bf16_f32 v0, v4, v5
	v_cvt_pk_bf16_f32 v1, v6, v7
	s_nop 0
	v_cvt_pk_bf16_f32 v2, v2, v3
	v_cvt_pk_bf16_f32 v3, v8, v9
	ds_write_b128 v186, v[0:3]
	ds_read_b128 v[202:205], v187
	v_mov_b64_e32 v[216:217], v[12:13]
	s_waitcnt lgkmcnt(4)
	global_store_dwordx4 v[214:215], v[190:193], off
	global_store_dwordx4 v[214:215], v[194:197], off offset:256
	s_waitcnt lgkmcnt(0)
	global_store_dwordx4 v[216:217], v[198:201], off
	global_store_dwordx4 v[216:217], v[202:205], off offset:256
	s_and_b64 vcc, exec, s[2:3]
	s_mov_b64 s[2:3], -1
	s_cbranch_vccnz .LBB0_228
